# variant: cached-block stores with default cache policy (stay in L2) instead of write-through
# baseline (speedup 1.0000x reference)
.LBB2_50:
	s_andn2_b64 vcc, exec, s[16:17]
	s_cbranch_vccnz .LBB2_55
	v_max_f32_e32 v2, v100, v100
	v_max_f32_e32 v2, 0xc6ea6000, v2
	v_and_b32_e32 v4, 0xffff0000, v2
	v_and_b32_e32 v3, 0xffff0000, v99
	v_sub_f32_e32 v5, v2, v4
	v_sub_f32_e32 v3, v99, v3
	v_and_b32_e32 v6, 0xffff0000, v5
	s_mov_b32 s16, 0xffff0000
	v_and_b32_e32 v3, 0xffff0000, v3
	v_sub_f32_e32 v6, v5, v6
	v_lshrrev_b32_e32 v5, 16, v5
	v_or_b32_sdwa v109, v4, v99 dst_sel:DWORD dst_unused:UNUSED_PAD src0_sel:DWORD src1_sel:WORD_1
	v_or_b32_sdwa v108, v3, v99 dst_sel:DWORD dst_unused:UNUSED_PAD src0_sel:DWORD src1_sel:WORD_1
	v_and_or_b32 v110, v6, s16, v5
	v_or_b32_sdwa v111, v2, v4 dst_sel:DWORD dst_unused:UNUSED_PAD src0_sel:WORD_1 src1_sel:DWORD
	s_movk_i32 s16, 0xfc00
	s_nop 0
	v_mfma_f32_32x32x16_bf16 v[2:17], v[40:43], v[108:111], 0
	s_nop 11
	v_cvt_pk_f16_f32 v2, v2, v3
	v_cvt_pk_f16_f32 v3, v4, v5
	v_pk_max_i16 v2, v2, s16 op_sel_hi:[1,0]
	v_pk_max_i16 v3, v3, s16 op_sel_hi:[1,0]
	s_nop 0
	v_exp_f16_e32 v100, v2
	v_exp_f16_e32 v99, v3
	v_exp_f16_sdwa v100, v2 dst_sel:WORD_1 dst_unused:UNUSED_PRESERVE src0_sel:WORD_1
	v_exp_f16_sdwa v99, v3 dst_sel:WORD_1 dst_unused:UNUSED_PRESERVE src0_sel:WORD_1
	v_cvt_pk_f16_f32 v2, v6, v7
	v_cvt_pk_f16_f32 v3, v8, v9
	v_pk_max_i16 v2, v2, s16 op_sel_hi:[1,0]
	v_pk_max_i16 v3, v3, s16 op_sel_hi:[1,0]
	s_nop 0
	v_exp_f16_e32 v102, v2
	v_exp_f16_e32 v101, v3
	v_exp_f16_sdwa v102, v2 dst_sel:WORD_1 dst_unused:UNUSED_PRESERVE src0_sel:WORD_1
	v_exp_f16_sdwa v101, v3 dst_sel:WORD_1 dst_unused:UNUSED_PRESERVE src0_sel:WORD_1
	v_cvt_pk_f16_f32 v2, v10, v11
	v_cvt_pk_f16_f32 v3, v12, v13
	v_pk_max_i16 v2, v2, s16 op_sel_hi:[1,0]
	v_pk_max_i16 v3, v3, s16 op_sel_hi:[1,0]
	s_nop 0
	v_exp_f16_e32 v104, v2
	v_exp_f16_e32 v103, v3
	v_exp_f16_sdwa v104, v2 dst_sel:WORD_1 dst_unused:UNUSED_PRESERVE src0_sel:WORD_1
	v_exp_f16_sdwa v103, v3 dst_sel:WORD_1 dst_unused:UNUSED_PRESERVE src0_sel:WORD_1
	v_cvt_pk_f16_f32 v2, v14, v15
	v_cvt_pk_f16_f32 v3, v16, v17
	v_pk_max_i16 v2, v2, s16 op_sel_hi:[1,0]
	v_pk_max_i16 v3, v3, s16 op_sel_hi:[1,0]
	s_nop 0
	v_exp_f16_e32 v106, v2
	v_exp_f16_e32 v105, v3
	v_exp_f16_sdwa v106, v2 dst_sel:WORD_1 dst_unused:UNUSED_PRESERVE src0_sel:WORD_1
	v_exp_f16_sdwa v105, v3 dst_sel:WORD_1 dst_unused:UNUSED_PRESERVE src0_sel:WORD_1
	v_mfma_f32_32x32x16_bf16 v[2:17], v[36:39], v[108:111], 0
	s_nop 11
	v_cvt_pk_f16_f32 v2, v2, v3
	v_cvt_pk_f16_f32 v3, v4, v5
	v_pk_max_i16 v2, v2, s16 op_sel_hi:[1,0]
	v_pk_max_i16 v3, v3, s16 op_sel_hi:[1,0]
	s_nop 0
	v_exp_f16_e32 v108, v2
	v_exp_f16_e32 v107, v3
	v_exp_f16_sdwa v108, v2 dst_sel:WORD_1 dst_unused:UNUSED_PRESERVE src0_sel:WORD_1
	v_exp_f16_sdwa v107, v3 dst_sel:WORD_1 dst_unused:UNUSED_PRESERVE src0_sel:WORD_1
	v_cvt_pk_f16_f32 v2, v6, v7
	v_cvt_pk_f16_f32 v3, v8, v9
	v_pk_max_i16 v2, v2, s16 op_sel_hi:[1,0]
	v_pk_max_i16 v3, v3, s16 op_sel_hi:[1,0]
	s_nop 0
	v_exp_f16_e32 v110, v2
	v_exp_f16_e32 v109, v3
	v_exp_f16_sdwa v110, v2 dst_sel:WORD_1 dst_unused:UNUSED_PRESERVE src0_sel:WORD_1
	v_exp_f16_sdwa v109, v3 dst_sel:WORD_1 dst_unused:UNUSED_PRESERVE src0_sel:WORD_1
	v_cvt_pk_f16_f32 v2, v10, v11
	v_cvt_pk_f16_f32 v3, v12, v13
	v_pk_max_i16 v2, v2, s16 op_sel_hi:[1,0]
	v_pk_max_i16 v3, v3, s16 op_sel_hi:[1,0]
	s_nop 0
	v_exp_f16_e32 v112, v2
	v_exp_f16_e32 v111, v3
	v_exp_f16_sdwa v112, v2 dst_sel:WORD_1 dst_unused:UNUSED_PRESERVE src0_sel:WORD_1
	v_exp_f16_sdwa v111, v3 dst_sel:WORD_1 dst_unused:UNUSED_PRESERVE src0_sel:WORD_1
	v_cvt_pk_f16_f32 v2, v14, v15
	v_cvt_pk_f16_f32 v3, v16, v17
	v_pk_max_i16 v2, v2, s16 op_sel_hi:[1,0]
	v_pk_max_i16 v3, v3, s16 op_sel_hi:[1,0]
	s_mov_b64 s[16:17], -1
	v_exp_f16_e32 v114, v2
	v_exp_f16_e32 v113, v3
	v_exp_f16_sdwa v114, v2 dst_sel:WORD_1 dst_unused:UNUSED_PRESERVE src0_sel:WORD_1
	v_exp_f16_sdwa v113, v3 dst_sel:WORD_1 dst_unused:UNUSED_PRESERVE src0_sel:WORD_1
	s_cmpk_gt_i32 s60, 0x800
	s_cbranch_scc1 .Lfirst_nocache1
	s_lshl_b32 s66, s46, 16
	s_add_u32 s66, s98, s66
	s_addc_u32 s67, s99, 0
	s_lshl_b32 s68, s27, 12
	s_add_u32 s68, s68, 0x8000
	s_add_u32 s66, s66, s68
	s_addc_u32 s67, s67, 0
	v_lshlrev_b32_e32 v216, 4, v44
	v_mov_b32_e32 v236, v100
	v_mov_b32_e32 v237, v99
	v_mov_b32_e32 v238, v102
	v_mov_b32_e32 v239, v101
	v_mov_b32_e32 v240, v104
	v_mov_b32_e32 v241, v103
	v_mov_b32_e32 v242, v106
	v_mov_b32_e32 v243, v105
	v_mov_b32_e32 v244, v108
	v_mov_b32_e32 v245, v107
	v_mov_b32_e32 v246, v110
	v_mov_b32_e32 v247, v109
	v_mov_b32_e32 v248, v112
	v_mov_b32_e32 v249, v111
	v_mov_b32_e32 v250, v114
	v_mov_b32_e32 v251, v113
	global_store_dwordx4 v216, v[236:239], s[66:67]
	global_store_dwordx4 v216, v[240:243], s[66:67] offset:1024
	global_store_dwordx4 v216, v[244:247], s[66:67] offset:2048
	global_store_dwordx4 v216, v[248:251], s[66:67] offset:3072

.LBB2_53:
	v_max_f32_e32 v2, v115, v115
	v_max_f32_e32 v2, 0xc6ea6000, v2
	v_and_b32_e32 v4, 0xffff0000, v2
	v_and_b32_e32 v3, 0xffff0000, v1
	v_sub_f32_e32 v5, v2, v4
	v_sub_f32_e32 v3, v1, v3
	v_and_b32_e32 v6, 0xffff0000, v5
	s_mov_b32 s0, 0xffff0000
	v_and_b32_e32 v3, 0xffff0000, v3
	v_sub_f32_e32 v6, v5, v6
	v_lshrrev_b32_e32 v5, 16, v5
	v_or_b32_sdwa v117, v4, v1 dst_sel:DWORD dst_unused:UNUSED_PAD src0_sel:DWORD src1_sel:WORD_1
	v_or_b32_sdwa v116, v3, v1 dst_sel:DWORD dst_unused:UNUSED_PAD src0_sel:DWORD src1_sel:WORD_1
	v_and_or_b32 v118, v6, s0, v5
	v_or_b32_sdwa v119, v2, v4 dst_sel:DWORD dst_unused:UNUSED_PAD src0_sel:WORD_1 src1_sel:DWORD
	s_movk_i32 s0, 0xfc00
	s_nop 0
	v_mfma_f32_32x32x16_bf16 v[2:17], v[40:43], v[116:119], 0
	s_nop 11
	v_cvt_pk_f16_f32 v1, v2, v3
	v_cvt_pk_f16_f32 v2, v4, v5
	v_pk_max_i16 v2, v2, s0 op_sel_hi:[1,0]
	v_pk_max_i16 v1, v1, s0 op_sel_hi:[1,0]
	s_nop 0
	v_exp_f16_e32 v130, v1
	v_exp_f16_e32 v127, v2
	v_exp_f16_sdwa v130, v1 dst_sel:WORD_1 dst_unused:UNUSED_PRESERVE src0_sel:WORD_1
	v_exp_f16_sdwa v127, v2 dst_sel:WORD_1 dst_unused:UNUSED_PRESERVE src0_sel:WORD_1
	v_cvt_pk_f16_f32 v2, v8, v9
	v_cvt_pk_f16_f32 v1, v6, v7
	v_pk_max_i16 v2, v2, s0 op_sel_hi:[1,0]
	v_pk_max_i16 v1, v1, s0 op_sel_hi:[1,0]
	s_nop 0
	v_exp_f16_e32 v129, v1
	v_exp_f16_e32 v124, v2
	v_exp_f16_sdwa v129, v1 dst_sel:WORD_1 dst_unused:UNUSED_PRESERVE src0_sel:WORD_1
	v_exp_f16_sdwa v124, v2 dst_sel:WORD_1 dst_unused:UNUSED_PRESERVE src0_sel:WORD_1
	v_cvt_pk_f16_f32 v2, v12, v13
	v_cvt_pk_f16_f32 v1, v10, v11
	v_pk_max_i16 v2, v2, s0 op_sel_hi:[1,0]
	v_pk_max_i16 v1, v1, s0 op_sel_hi:[1,0]
	s_nop 0
	v_exp_f16_e32 v128, v1
	v_exp_f16_e32 v122, v2
	v_exp_f16_sdwa v128, v1 dst_sel:WORD_1 dst_unused:UNUSED_PRESERVE src0_sel:WORD_1
	v_exp_f16_sdwa v122, v2 dst_sel:WORD_1 dst_unused:UNUSED_PRESERVE src0_sel:WORD_1
	v_cvt_pk_f16_f32 v2, v16, v17
	v_cvt_pk_f16_f32 v1, v14, v15
	v_pk_max_i16 v2, v2, s0 op_sel_hi:[1,0]
	v_pk_max_i16 v1, v1, s0 op_sel_hi:[1,0]
	s_nop 0
	v_exp_f16_e32 v126, v1
	v_exp_f16_e32 v120, v2
	v_exp_f16_sdwa v126, v1 dst_sel:WORD_1 dst_unused:UNUSED_PRESERVE src0_sel:WORD_1
	v_exp_f16_sdwa v120, v2 dst_sel:WORD_1 dst_unused:UNUSED_PRESERVE src0_sel:WORD_1
	v_mfma_f32_32x32x16_bf16 v[2:17], v[36:39], v[116:119], 0
	s_nop 11
	v_cvt_pk_f16_f32 v1, v2, v3
	v_cvt_pk_f16_f32 v2, v4, v5
	v_pk_max_i16 v1, v1, s0 op_sel_hi:[1,0]
	v_pk_max_i16 v2, v2, s0 op_sel_hi:[1,0]
	s_nop 0
	v_exp_f16_e32 v125, v1
	v_exp_f16_e32 v119, v2
	v_exp_f16_sdwa v125, v1 dst_sel:WORD_1 dst_unused:UNUSED_PRESERVE src0_sel:WORD_1
	v_exp_f16_sdwa v119, v2 dst_sel:WORD_1 dst_unused:UNUSED_PRESERVE src0_sel:WORD_1
	v_cvt_pk_f16_f32 v1, v6, v7
	v_cvt_pk_f16_f32 v2, v8, v9
	v_pk_max_i16 v1, v1, s0 op_sel_hi:[1,0]
	v_pk_max_i16 v2, v2, s0 op_sel_hi:[1,0]
	s_nop 0
	v_exp_f16_e32 v123, v1
	v_exp_f16_e32 v117, v2
	v_exp_f16_sdwa v123, v1 dst_sel:WORD_1 dst_unused:UNUSED_PRESERVE src0_sel:WORD_1
	v_exp_f16_sdwa v117, v2 dst_sel:WORD_1 dst_unused:UNUSED_PRESERVE src0_sel:WORD_1
	v_cvt_pk_f16_f32 v1, v10, v11
	v_cvt_pk_f16_f32 v2, v12, v13
	v_pk_max_i16 v1, v1, s0 op_sel_hi:[1,0]
	v_pk_max_i16 v2, v2, s0 op_sel_hi:[1,0]
	s_nop 0
	v_exp_f16_e32 v121, v1
	v_exp_f16_e32 v116, v2
	v_exp_f16_sdwa v121, v1 dst_sel:WORD_1 dst_unused:UNUSED_PRESERVE src0_sel:WORD_1
	v_exp_f16_sdwa v116, v2 dst_sel:WORD_1 dst_unused:UNUSED_PRESERVE src0_sel:WORD_1
	v_cvt_pk_f16_f32 v1, v14, v15
	v_cvt_pk_f16_f32 v2, v16, v17
	v_pk_max_i16 v1, v1, s0 op_sel_hi:[1,0]
	v_pk_max_i16 v2, v2, s0 op_sel_hi:[1,0]
	s_nop 0
	v_exp_f16_e32 v118, v1
	v_exp_f16_e32 v17, v2
	v_exp_f16_sdwa v118, v1 dst_sel:WORD_1 dst_unused:UNUSED_PRESERVE src0_sel:WORD_1
	v_exp_f16_sdwa v17, v2 dst_sel:WORD_1 dst_unused:UNUSED_PRESERVE src0_sel:WORD_1
	s_cmpk_gt_i32 s38, 0x800
	s_cbranch_scc1 .Lfirst_nocache
	s_lshl_b32 s66, s27, 12
	s_add_u32 s66, s66, 0x8000
	s_add_u32 s66, s44, s66
	s_addc_u32 s67, s45, 0
	v_lshlrev_b32_e32 v216, 4, v44
	v_mov_b32_e32 v220, v130
	v_mov_b32_e32 v221, v127
	v_mov_b32_e32 v222, v129
	v_mov_b32_e32 v223, v124
	v_mov_b32_e32 v224, v128
	v_mov_b32_e32 v225, v122
	v_mov_b32_e32 v226, v126
	v_mov_b32_e32 v227, v120
	v_mov_b32_e32 v228, v125
	v_mov_b32_e32 v229, v119
	v_mov_b32_e32 v230, v123
	v_mov_b32_e32 v231, v117
	v_mov_b32_e32 v232, v121
	v_mov_b32_e32 v233, v116
	v_mov_b32_e32 v234, v118
	v_mov_b32_e32 v235, v17
	global_store_dwordx4 v216, v[220:223], s[66:67]
	global_store_dwordx4 v216, v[224:227], s[66:67] offset:1024
	global_store_dwordx4 v216, v[228:231], s[66:67] offset:2048
	global_store_dwordx4 v216, v[232:235], s[66:67] offset:3072
